# prep kk-norm: dead shuffle-index computations removed (the DPP moves overwrite the index register)
# baseline (speedup 1.0000x reference)
.LBB0_491:
	v_cndmask_b32_e64 v90, 0, 1, s[58:59]
	s_and_b64 vcc, exec, s[4:5]
	v_lshl_add_u64 v[62:63], s[50:51], 0, v[86:87]
	v_cmp_ne_u32_e64 s[42:43], 1, v90
	s_cbranch_vccz .LBB0_494
	v_add_co_u32_e32 v90, vcc, 0x2e200000, v62
	v_cvt_pk_bf16_f32 v124, v120, v121
	v_cvt_pk_bf16_f32 v125, v122, v123
	v_cvt_pk_bf16_f32 v126, v98, v99
	v_cvt_pk_bf16_f32 v127, v64, v65
	s_nop 1
	v_addc_co_u32_e32 v91, vcc, 0, v63, vcc
	s_and_b64 vcc, exec, s[42:43]
	global_store_dwordx4 v[90:91], v[124:127], off sc1
	s_cbranch_vccnz .LBB0_494
	v_mul_f32_e32 v121, v103, v121
	v_mul_f32_e32 v120, v104, v120
	v_mul_f32_e32 v124, v121, v121
	v_fmac_f32_e32 v124, v120, v120
	v_mul_f32_e32 v122, v110, v122
	v_fmac_f32_e32 v124, v122, v122
	v_mul_f32_e32 v123, v109, v123
	v_pk_mul_f32 v[90:91], v[72:73], v[98:99]
	v_fmac_f32_e32 v124, v123, v123
	v_pk_mul_f32 v[98:99], v[90:91], v[90:91]
	v_pk_mul_f32 v[64:65], v[78:79], v[64:65]
	v_add_f32_e32 v98, v98, v124
	v_add_f32_e32 v124, v99, v98
	v_pk_mul_f32 v[98:99], v[64:65], v[64:65]
	s_nop 0
	v_add_f32_e32 v98, v98, v124
	v_and_b32_e32 v124, 64, v226
	v_add_f32_e32 v98, v99, v98
	v_xor_b32_e32 v99, 1, v226
	v_add_u32_e32 v124, 64, v124
	v_cmp_lt_i32_e32 vcc, v99, v124
	s_nop 1
	v_cndmask_b32_e32 v99, v226, v99, vcc
	v_lshlrev_b32_e32 v99, 2, v99
	v_mov_b32_dpp v99, v98 quad_perm:[1,0,3,2] row_mask:0xf bank_mask:0xf
	s_waitcnt lgkmcnt(0)
	v_add_f32_e32 v98, v98, v99
	s_nop 1
	v_mov_b32_dpp v99, v98 quad_perm:[2,3,0,1] row_mask:0xf bank_mask:0xf
	s_waitcnt lgkmcnt(0)
	v_add_f32_e32 v98, v98, v99
	s_nop 1
	v_mov_b32_dpp v99, v98 row_half_mirror row_mask:0xf bank_mask:0xf
	s_waitcnt lgkmcnt(0)
	v_add_f32_e32 v98, v98, v99
	v_mul_f32_e32 v99, 0x4f800000, v98
	v_cmp_gt_f32_e32 vcc, s82, v98
	s_nop 1
	v_cndmask_b32_e32 v98, v98, v99, vcc
	v_sqrt_f32_e32 v99, v98
	s_nop 0
	v_add_u32_e32 v124, -1, v99
	v_fma_f32 v125, -v124, v99, v98
	v_cmp_ge_f32_e64 s[46:47], 0, v125
	v_add_u32_e32 v125, 1, v99
	s_nop 0
	v_cndmask_b32_e64 v124, v99, v124, s[46:47]
	v_fma_f32 v99, -v125, v99, v98
	v_cmp_lt_f32_e64 s[46:47], 0, v99
	s_nop 1
	v_cndmask_b32_e64 v99, v124, v125, s[46:47]
	v_mul_f32_e32 v124, 0x37800000, v99
	v_cndmask_b32_e32 v99, v99, v124, vcc
	v_cmp_class_f32_e32 vcc, v98, v229
	s_nop 1
	v_cndmask_b32_e32 v98, v99, v98, vcc
	v_max_f32_e32 v98, 0x2b8cbccc, v98
	v_div_scale_f32 v99, s[4:5], v98, v98, 1.0
	v_rcp_f32_e32 v124, v99
	s_nop 0
	v_fma_f32 v125, -v99, v124, 1.0
	v_fmac_f32_e32 v124, v125, v124
	v_div_scale_f32 v125, vcc, 1.0, v98, 1.0
	v_mul_f32_e32 v126, v125, v124
	v_fma_f32 v127, -v99, v126, v125
	v_fmac_f32_e32 v126, v127, v124
	v_fma_f32 v99, -v99, v126, v125
	v_div_fmas_f32 v99, v99, v124, v126
	v_div_fixup_f32 v98, v99, v98, 1.0
	v_mul_f32_e32 v99, v120, v98
	v_mul_f32_e32 v120, v121, v98
	v_mul_f32_e32 v121, v122, v98
	v_mul_f32_e32 v122, v123, v98
	v_mul_f32_e32 v64, v64, v98
	v_mul_f32_e32 v65, v65, v98
	v_mul_f32_e32 v90, v90, v98
	v_mul_f32_e32 v91, v91, v98
	v_cvt_pk_bf16_f32 v120, v99, v120
	v_cvt_pk_bf16_f32 v121, v121, v122
	v_cvt_pk_bf16_f32 v122, v90, v91
	v_cvt_pk_bf16_f32 v123, v64, v65
	v_lshl_add_u64 v[64:65], s[50:51], 0, v[84:85]
	v_add_co_u32_e32 v64, vcc, 0x2e201000, v64
	s_nop 1
	v_addc_co_u32_e32 v65, vcc, 0, v65, vcc
	global_store_dwordx4 v[64:65], v[120:123], off offset:2048 sc1

.LBB0_528:
	s_and_b64 vcc, exec, s[4:5]
	s_cbranch_vccz .LBB0_531
	v_add_co_u32_e32 v122, vcc, 0x2e202000, v62
	v_cvt_pk_bf16_f32 v92, v115, v114
	v_cvt_pk_bf16_f32 v93, v113, v0
	v_cvt_pk_bf16_f32 v94, v58, v59
	v_cvt_pk_bf16_f32 v95, v60, v61
	s_nop 1
	v_addc_co_u32_e32 v123, vcc, 0, v63, vcc
	s_and_b64 vcc, exec, s[42:43]
	global_store_dwordx4 v[122:123], v[92:95], off sc1
	s_cbranch_vccnz .LBB0_531
	s_nop 0
	v_mul_f32_e32 v95, v103, v114
	v_mul_f32_e32 v94, v104, v115
	v_mul_f32_e32 v114, v95, v95
	v_fmac_f32_e32 v114, v94, v94
	v_mul_f32_e32 v113, v110, v113
	v_fmac_f32_e32 v114, v113, v113
	v_mul_f32_e32 v0, v109, v0
	v_pk_mul_f32 v[58:59], v[72:73], v[58:59]
	v_fmac_f32_e32 v114, v0, v0
	v_pk_mul_f32 v[92:93], v[58:59], v[58:59]
	v_pk_mul_f32 v[60:61], v[78:79], v[60:61]
	v_add_f32_e32 v92, v92, v114
	v_add_f32_e32 v114, v93, v92
	v_pk_mul_f32 v[92:93], v[60:61], v[60:61]
	s_nop 0
	v_add_f32_e32 v92, v92, v114
	v_and_b32_e32 v114, 64, v226
	v_add_f32_e32 v92, v93, v92
	v_xor_b32_e32 v93, 1, v226
	v_add_u32_e32 v114, 64, v114
	v_cmp_lt_i32_e32 vcc, v93, v114
	s_nop 1
	v_cndmask_b32_e32 v93, v226, v93, vcc
	v_lshlrev_b32_e32 v93, 2, v93
	v_mov_b32_dpp v93, v92 quad_perm:[1,0,3,2] row_mask:0xf bank_mask:0xf
	s_waitcnt lgkmcnt(0)
	v_add_f32_e32 v92, v92, v93
	s_nop 1
	v_mov_b32_dpp v93, v92 quad_perm:[2,3,0,1] row_mask:0xf bank_mask:0xf
	s_waitcnt lgkmcnt(0)
	v_add_f32_e32 v92, v92, v93
	s_nop 1
	v_mov_b32_dpp v93, v92 row_half_mirror row_mask:0xf bank_mask:0xf
	s_waitcnt lgkmcnt(0)
	v_add_f32_e32 v92, v92, v93
	v_mul_f32_e32 v93, 0x4f800000, v92
	v_cmp_gt_f32_e32 vcc, s82, v92
	s_nop 1
	v_cndmask_b32_e32 v92, v92, v93, vcc
	v_sqrt_f32_e32 v93, v92
	s_nop 0
	v_add_u32_e32 v114, -1, v93
	v_fma_f32 v115, -v114, v93, v92
	v_cmp_ge_f32_e64 s[46:47], 0, v115
	v_add_u32_e32 v115, 1, v93
	s_nop 0
	v_cndmask_b32_e64 v114, v93, v114, s[46:47]
	v_fma_f32 v93, -v115, v93, v92
	v_cmp_lt_f32_e64 s[46:47], 0, v93
	s_nop 1
	v_cndmask_b32_e64 v93, v114, v115, s[46:47]
	v_mul_f32_e32 v114, 0x37800000, v93
	v_cndmask_b32_e32 v93, v93, v114, vcc
	v_cmp_class_f32_e32 vcc, v92, v229
	s_nop 1
	v_cndmask_b32_e32 v92, v93, v92, vcc
	v_max_f32_e32 v92, 0x2b8cbccc, v92
	v_div_scale_f32 v93, s[4:5], v92, v92, 1.0
	v_rcp_f32_e32 v114, v93
	s_nop 0
	v_fma_f32 v115, -v93, v114, 1.0
	v_fmac_f32_e32 v114, v115, v114
	v_div_scale_f32 v115, vcc, 1.0, v92, 1.0
	v_mul_f32_e32 v122, v115, v114
	v_fma_f32 v123, -v93, v122, v115
	v_fmac_f32_e32 v122, v123, v114
	v_fma_f32 v93, -v93, v122, v115
	v_div_fmas_f32 v93, v93, v114, v122
	v_div_fixup_f32 v92, v93, v92, 1.0
	v_mul_f32_e32 v93, v94, v92
	v_mul_f32_e32 v94, v95, v92
	v_mul_f32_e32 v95, v113, v92
	v_mul_f32_e32 v0, v0, v92
	v_mul_f32_e32 v113, v58, v92
	v_mul_f32_e32 v114, v59, v92
	v_mul_f32_e32 v115, v60, v92
	v_mul_f32_e32 v61, v61, v92
	v_cvt_pk_bf16_f32 v58, v93, v94
	v_lshl_add_u64 v[92:93], s[50:51], 0, v[84:85]
	v_add_co_u32_e32 v92, vcc, 0x2e203000, v92
	v_cvt_pk_bf16_f32 v59, v95, v0
	v_cvt_pk_bf16_f32 v60, v113, v114
	v_cvt_pk_bf16_f32 v61, v115, v61
	s_nop 1
	v_addc_co_u32_e32 v93, vcc, 0, v93, vcc
	global_store_dwordx4 v[92:93], v[58:61], off offset:2048 sc1

.LBB0_565:
	s_and_b64 vcc, exec, s[4:5]
	s_cbranch_vccz .LBB0_568
	v_add_co_u32_e32 v88, vcc, 0x2e204000, v62
	v_cvt_pk_bf16_f32 v116, v94, v113
	v_cvt_pk_bf16_f32 v117, v114, v115
	v_cvt_pk_bf16_f32 v118, v54, v55
	v_cvt_pk_bf16_f32 v119, v56, v57
	s_nop 1
	v_addc_co_u32_e32 v89, vcc, 0, v63, vcc
	s_and_b64 vcc, exec, s[42:43]
	global_store_dwordx4 v[88:89], v[116:119], off sc1
	s_cbranch_vccnz .LBB0_568
	v_mul_f32_e32 v96, v103, v113
	v_mul_f32_e32 v94, v104, v94
	v_mul_f32_e32 v97, v96, v96
	v_fmac_f32_e32 v97, v94, v94
	v_mul_f32_e32 v113, v110, v114
	v_fmac_f32_e32 v97, v113, v113
	v_mul_f32_e32 v114, v109, v115
	v_pk_mul_f32 v[54:55], v[72:73], v[54:55]
	v_fmac_f32_e32 v97, v114, v114
	v_pk_mul_f32 v[88:89], v[54:55], v[54:55]
	v_pk_mul_f32 v[56:57], v[78:79], v[56:57]
	v_add_f32_e32 v88, v88, v97
	v_add_f32_e32 v97, v89, v88
	v_pk_mul_f32 v[88:89], v[56:57], v[56:57]
	s_nop 0
	v_add_f32_e32 v88, v88, v97
	v_and_b32_e32 v97, 64, v226
	v_add_f32_e32 v88, v89, v88
	v_xor_b32_e32 v89, 1, v226
	v_add_u32_e32 v97, 64, v97
	v_cmp_lt_i32_e32 vcc, v89, v97
	s_nop 1
	v_cndmask_b32_e32 v89, v226, v89, vcc
	v_lshlrev_b32_e32 v89, 2, v89
	v_mov_b32_dpp v89, v88 quad_perm:[1,0,3,2] row_mask:0xf bank_mask:0xf
	s_waitcnt lgkmcnt(0)
	v_add_f32_e32 v88, v88, v89
	s_nop 1
	v_mov_b32_dpp v89, v88 quad_perm:[2,3,0,1] row_mask:0xf bank_mask:0xf
	s_waitcnt lgkmcnt(0)
	v_add_f32_e32 v88, v88, v89
	s_nop 1
	v_mov_b32_dpp v89, v88 row_half_mirror row_mask:0xf bank_mask:0xf
	s_waitcnt lgkmcnt(0)
	v_add_f32_e32 v88, v88, v89
	v_mul_f32_e32 v89, 0x4f800000, v88
	v_cmp_gt_f32_e32 vcc, s82, v88
	s_nop 1
	v_cndmask_b32_e32 v88, v88, v89, vcc
	v_sqrt_f32_e32 v89, v88
	s_nop 0
	v_add_u32_e32 v97, -1, v89
	v_fma_f32 v115, -v97, v89, v88
	v_cmp_ge_f32_e64 s[46:47], 0, v115
	v_add_u32_e32 v115, 1, v89
	s_nop 0
	v_cndmask_b32_e64 v97, v89, v97, s[46:47]
	v_fma_f32 v89, -v115, v89, v88
	v_cmp_lt_f32_e64 s[46:47], 0, v89
	s_nop 1
	v_cndmask_b32_e64 v89, v97, v115, s[46:47]
	v_mul_f32_e32 v97, 0x37800000, v89
	v_cndmask_b32_e32 v89, v89, v97, vcc
	v_cmp_class_f32_e32 vcc, v88, v229
	s_nop 1
	v_cndmask_b32_e32 v88, v89, v88, vcc
	v_max_f32_e32 v88, 0x2b8cbccc, v88
	v_div_scale_f32 v89, s[4:5], v88, v88, 1.0
	v_rcp_f32_e32 v97, v89
	s_nop 0
	v_fma_f32 v115, -v89, v97, 1.0
	v_fmac_f32_e32 v97, v115, v97
	v_div_scale_f32 v115, vcc, 1.0, v88, 1.0
	v_mul_f32_e32 v116, v115, v97
	v_fma_f32 v117, -v89, v116, v115
	v_fmac_f32_e32 v116, v117, v97
	v_fma_f32 v89, -v89, v116, v115
	v_div_fmas_f32 v89, v89, v97, v116
	v_div_fixup_f32 v88, v89, v88, 1.0
	v_mul_f32_e32 v89, v94, v88
	v_mul_f32_e32 v94, v96, v88
	v_mul_f32_e32 v96, v113, v88
	v_mul_f32_e32 v97, v114, v88
	v_mul_f32_e32 v113, v54, v88
	v_mul_f32_e32 v114, v55, v88
	v_mul_f32_e32 v115, v56, v88
	v_mul_f32_e32 v57, v57, v88
	v_cvt_pk_bf16_f32 v54, v89, v94
	v_lshl_add_u64 v[88:89], s[50:51], 0, v[84:85]
	v_add_co_u32_e32 v88, vcc, 0x2e205000, v88
	v_cvt_pk_bf16_f32 v55, v96, v97
	v_cvt_pk_bf16_f32 v56, v113, v114
	v_cvt_pk_bf16_f32 v57, v115, v57
	s_nop 1
	v_addc_co_u32_e32 v89, vcc, 0, v89, vcc
	global_store_dwordx4 v[88:89], v[54:57], off offset:2048 sc1

.LBB0_602:
	s_and_b64 vcc, exec, s[4:5]
	s_cbranch_vccz .LBB0_605
	v_add_co_u32_e32 v64, vcc, 0x2e206000, v62
	v_cvt_pk_bf16_f32 v114, v97, v113
	v_cvt_pk_bf16_f32 v115, v99, v98
	v_cvt_pk_bf16_f32 v116, v50, v51
	v_cvt_pk_bf16_f32 v117, v52, v53
	s_nop 1
	v_addc_co_u32_e32 v65, vcc, 0, v63, vcc
	s_and_b64 vcc, exec, s[42:43]
	global_store_dwordx4 v[64:65], v[114:117], off sc1
	s_cbranch_vccnz .LBB0_605
	v_mul_f32_e32 v91, v103, v113
	v_mul_f32_e32 v90, v104, v97
	v_mul_f32_e32 v97, v91, v91
	v_fmac_f32_e32 v97, v90, v90
	v_mul_f32_e32 v99, v110, v99
	v_fmac_f32_e32 v97, v99, v99
	v_mul_f32_e32 v98, v109, v98
	v_pk_mul_f32 v[50:51], v[72:73], v[50:51]
	v_fmac_f32_e32 v97, v98, v98
	v_pk_mul_f32 v[64:65], v[50:51], v[50:51]
	v_pk_mul_f32 v[52:53], v[78:79], v[52:53]
	v_add_f32_e32 v64, v64, v97
	v_add_f32_e32 v97, v65, v64
	v_pk_mul_f32 v[64:65], v[52:53], v[52:53]
	s_nop 0
	v_add_f32_e32 v64, v64, v97
	v_and_b32_e32 v97, 64, v226
	v_add_f32_e32 v64, v65, v64
	v_xor_b32_e32 v65, 1, v226
	v_add_u32_e32 v97, 64, v97
	v_cmp_lt_i32_e32 vcc, v65, v97
	s_nop 1
	v_cndmask_b32_e32 v65, v226, v65, vcc
	v_lshlrev_b32_e32 v65, 2, v65
	v_mov_b32_dpp v65, v64 quad_perm:[1,0,3,2] row_mask:0xf bank_mask:0xf
	s_waitcnt lgkmcnt(0)
	v_add_f32_e32 v64, v64, v65
	s_nop 1
	v_mov_b32_dpp v65, v64 quad_perm:[2,3,0,1] row_mask:0xf bank_mask:0xf
	s_waitcnt lgkmcnt(0)
	v_add_f32_e32 v64, v64, v65
	s_nop 1
	v_mov_b32_dpp v65, v64 row_half_mirror row_mask:0xf bank_mask:0xf
	s_waitcnt lgkmcnt(0)
	v_add_f32_e32 v64, v64, v65
	v_mul_f32_e32 v65, 0x4f800000, v64
	v_cmp_gt_f32_e32 vcc, s82, v64
	s_nop 1
	v_cndmask_b32_e32 v64, v64, v65, vcc
	v_sqrt_f32_e32 v65, v64
	s_nop 0
	v_add_u32_e32 v97, -1, v65
	v_fma_f32 v113, -v97, v65, v64
	v_cmp_ge_f32_e64 s[46:47], 0, v113
	v_add_u32_e32 v113, 1, v65
	s_nop 0
	v_cndmask_b32_e64 v97, v65, v97, s[46:47]
	v_fma_f32 v65, -v113, v65, v64
	v_cmp_lt_f32_e64 s[46:47], 0, v65
	s_nop 1
	v_cndmask_b32_e64 v65, v97, v113, s[46:47]
	v_mul_f32_e32 v97, 0x37800000, v65
	v_cndmask_b32_e32 v65, v65, v97, vcc
	v_cmp_class_f32_e32 vcc, v64, v229
	s_nop 1
	v_cndmask_b32_e32 v64, v65, v64, vcc
	v_max_f32_e32 v64, 0x2b8cbccc, v64
	v_div_scale_f32 v65, s[4:5], v64, v64, 1.0
	v_rcp_f32_e32 v97, v65
	s_nop 0
	v_fma_f32 v113, -v65, v97, 1.0
	v_fmac_f32_e32 v97, v113, v97
	v_div_scale_f32 v113, vcc, 1.0, v64, 1.0
	v_mul_f32_e32 v114, v113, v97
	v_fma_f32 v115, -v65, v114, v113
	v_fmac_f32_e32 v114, v115, v97
	v_fma_f32 v65, -v65, v114, v113
	v_div_fmas_f32 v65, v65, v97, v114
	v_div_fixup_f32 v64, v65, v64, 1.0
	v_mul_f32_e32 v65, v90, v64
	v_mul_f32_e32 v90, v91, v64
	v_mul_f32_e32 v91, v99, v64
	v_mul_f32_e32 v97, v98, v64
	v_mul_f32_e32 v98, v50, v64
	v_mul_f32_e32 v99, v51, v64
	v_mul_f32_e32 v113, v52, v64
	v_mul_f32_e32 v53, v53, v64
	v_cvt_pk_bf16_f32 v50, v65, v90
	v_lshl_add_u64 v[64:65], s[50:51], 0, v[84:85]
	v_add_co_u32_e32 v64, vcc, 0x2e207000, v64
	v_cvt_pk_bf16_f32 v51, v91, v97
	v_cvt_pk_bf16_f32 v52, v98, v99
	v_cvt_pk_bf16_f32 v53, v113, v53
	s_nop 1
	v_addc_co_u32_e32 v65, vcc, 0, v65, vcc
	global_store_dwordx4 v[64:65], v[50:53], off offset:2048 sc1

.LBB0_639:
	s_and_b64 vcc, exec, s[4:5]
	s_cbranch_vccz .LBB0_642
	v_add_co_u32_e32 v98, vcc, 0x2e208000, v62
	v_cvt_pk_bf16_f32 v58, v95, v93
	v_cvt_pk_bf16_f32 v59, v92, v0
	v_cvt_pk_bf16_f32 v60, v46, v47
	v_cvt_pk_bf16_f32 v61, v48, v49
	s_nop 1
	v_addc_co_u32_e32 v99, vcc, 0, v63, vcc
	s_and_b64 vcc, exec, s[42:43]
	global_store_dwordx4 v[98:99], v[58:61], off sc1
	s_cbranch_vccnz .LBB0_642
	s_nop 0
	v_mul_f32_e32 v61, v103, v93
	v_mul_f32_e32 v60, v104, v95
	v_mul_f32_e32 v93, v61, v61
	v_fmac_f32_e32 v93, v60, v60
	v_mul_f32_e32 v92, v110, v92
	v_fmac_f32_e32 v93, v92, v92
	v_mul_f32_e32 v0, v109, v0
	v_pk_mul_f32 v[46:47], v[72:73], v[46:47]
	v_fmac_f32_e32 v93, v0, v0
	v_pk_mul_f32 v[58:59], v[46:47], v[46:47]
	v_pk_mul_f32 v[48:49], v[78:79], v[48:49]
	v_add_f32_e32 v58, v58, v93
	v_add_f32_e32 v93, v59, v58
	v_pk_mul_f32 v[58:59], v[48:49], v[48:49]
	s_nop 0
	v_add_f32_e32 v58, v58, v93
	v_and_b32_e32 v93, 64, v226
	v_add_f32_e32 v58, v59, v58
	v_xor_b32_e32 v59, 1, v226
	v_add_u32_e32 v93, 64, v93
	v_cmp_lt_i32_e32 vcc, v59, v93
	s_nop 1
	v_cndmask_b32_e32 v59, v226, v59, vcc
	v_lshlrev_b32_e32 v59, 2, v59
	v_mov_b32_dpp v59, v58 quad_perm:[1,0,3,2] row_mask:0xf bank_mask:0xf
	s_waitcnt lgkmcnt(0)
	v_add_f32_e32 v58, v58, v59
	s_nop 1
	v_mov_b32_dpp v59, v58 quad_perm:[2,3,0,1] row_mask:0xf bank_mask:0xf
	s_waitcnt lgkmcnt(0)
	v_add_f32_e32 v58, v58, v59
	s_nop 1
	v_mov_b32_dpp v59, v58 row_half_mirror row_mask:0xf bank_mask:0xf
	s_waitcnt lgkmcnt(0)
	v_add_f32_e32 v58, v58, v59
	v_mul_f32_e32 v59, 0x4f800000, v58
	v_cmp_gt_f32_e32 vcc, s82, v58
	s_nop 1
	v_cndmask_b32_e32 v58, v58, v59, vcc
	v_sqrt_f32_e32 v59, v58
	s_nop 0
	v_add_u32_e32 v93, -1, v59
	v_fma_f32 v95, -v93, v59, v58
	v_cmp_ge_f32_e64 s[46:47], 0, v95
	v_add_u32_e32 v95, 1, v59
	s_nop 0
	v_cndmask_b32_e64 v93, v59, v93, s[46:47]
	v_fma_f32 v59, -v95, v59, v58
	v_cmp_lt_f32_e64 s[46:47], 0, v59
	s_nop 1
	v_cndmask_b32_e64 v59, v93, v95, s[46:47]
	v_mul_f32_e32 v93, 0x37800000, v59
	v_cndmask_b32_e32 v59, v59, v93, vcc
	v_cmp_class_f32_e32 vcc, v58, v229
	s_nop 1
	v_cndmask_b32_e32 v58, v59, v58, vcc
	v_max_f32_e32 v58, 0x2b8cbccc, v58
	v_div_scale_f32 v59, s[4:5], v58, v58, 1.0
	v_rcp_f32_e32 v93, v59
	s_nop 0
	v_fma_f32 v95, -v59, v93, 1.0
	v_fmac_f32_e32 v93, v95, v93
	v_div_scale_f32 v95, vcc, 1.0, v58, 1.0
	v_mul_f32_e32 v97, v95, v93
	v_fma_f32 v98, -v59, v97, v95
	v_fmac_f32_e32 v97, v98, v93
	v_fma_f32 v59, -v59, v97, v95
	v_div_fmas_f32 v59, v59, v93, v97
	v_div_fixup_f32 v58, v59, v58, 1.0
	v_mul_f32_e32 v59, v60, v58
	v_mul_f32_e32 v60, v61, v58
	v_mul_f32_e32 v61, v92, v58
	v_mul_f32_e32 v0, v0, v58
	v_mul_f32_e32 v92, v46, v58
	v_mul_f32_e32 v93, v47, v58
	v_mul_f32_e32 v95, v48, v58
	v_mul_f32_e32 v49, v49, v58
	v_cvt_pk_bf16_f32 v46, v59, v60
	v_lshl_add_u64 v[58:59], s[50:51], 0, v[84:85]
	v_add_co_u32_e32 v58, vcc, 0x2e209000, v58
	v_cvt_pk_bf16_f32 v47, v61, v0
	v_cvt_pk_bf16_f32 v48, v92, v93
	v_cvt_pk_bf16_f32 v49, v95, v49
	s_nop 1
	v_addc_co_u32_e32 v59, vcc, 0, v59, vcc
	global_store_dwordx4 v[58:59], v[46:49], off offset:2048 sc1

.LBB0_676:
	s_and_b64 vcc, exec, s[4:5]
	s_cbranch_vccz .LBB0_679
	v_add_co_u32_e32 v94, vcc, 0x2e20a000, v62
	v_cvt_pk_bf16_f32 v54, v0, v92
	v_cvt_pk_bf16_f32 v55, v89, v88
	v_cvt_pk_bf16_f32 v56, v48, v49
	v_cvt_pk_bf16_f32 v57, v44, v45
	s_nop 1
	v_addc_co_u32_e32 v95, vcc, 0, v63, vcc
	s_and_b64 vcc, exec, s[42:43]
	global_store_dwordx4 v[94:95], v[54:57], off sc1
	s_cbranch_vccnz .LBB0_679
	s_nop 0
	v_mul_f32_e32 v56, v103, v92
	v_mul_f32_e32 v0, v104, v0
	v_mul_f32_e32 v57, v56, v56
	v_fmac_f32_e32 v57, v0, v0
	v_mul_f32_e32 v89, v110, v89
	v_fmac_f32_e32 v57, v89, v89
	v_mul_f32_e32 v88, v109, v88
	v_pk_mul_f32 v[48:49], v[72:73], v[48:49]
	v_fmac_f32_e32 v57, v88, v88
	v_pk_mul_f32 v[54:55], v[48:49], v[48:49]
	v_pk_mul_f32 v[44:45], v[78:79], v[44:45]
	v_add_f32_e32 v54, v54, v57
	v_add_f32_e32 v57, v55, v54
	v_pk_mul_f32 v[54:55], v[44:45], v[44:45]
	s_nop 0
	v_add_f32_e32 v54, v54, v57
	v_and_b32_e32 v57, 64, v226
	v_add_f32_e32 v54, v55, v54
	v_xor_b32_e32 v55, 1, v226
	v_add_u32_e32 v57, 64, v57
	v_cmp_lt_i32_e32 vcc, v55, v57
	s_nop 1
	v_cndmask_b32_e32 v55, v226, v55, vcc
	v_lshlrev_b32_e32 v55, 2, v55
	v_mov_b32_dpp v55, v54 quad_perm:[1,0,3,2] row_mask:0xf bank_mask:0xf
	s_waitcnt lgkmcnt(0)
	v_add_f32_e32 v54, v54, v55
	s_nop 1
	v_mov_b32_dpp v55, v54 quad_perm:[2,3,0,1] row_mask:0xf bank_mask:0xf
	s_waitcnt lgkmcnt(0)
	v_add_f32_e32 v54, v54, v55
	s_nop 1
	v_mov_b32_dpp v55, v54 row_half_mirror row_mask:0xf bank_mask:0xf
	s_waitcnt lgkmcnt(0)
	v_add_f32_e32 v54, v54, v55
	v_mul_f32_e32 v55, 0x4f800000, v54
	v_cmp_gt_f32_e32 vcc, s82, v54
	s_nop 1
	v_cndmask_b32_e32 v54, v54, v55, vcc
	v_sqrt_f32_e32 v55, v54
	s_nop 0
	v_add_u32_e32 v57, -1, v55
	v_fma_f32 v92, -v57, v55, v54
	v_cmp_ge_f32_e64 s[46:47], 0, v92
	v_add_u32_e32 v92, 1, v55
	s_nop 0
	v_cndmask_b32_e64 v57, v55, v57, s[46:47]
	v_fma_f32 v55, -v92, v55, v54
	v_cmp_lt_f32_e64 s[46:47], 0, v55
	s_nop 1
	v_cndmask_b32_e64 v55, v57, v92, s[46:47]
	v_mul_f32_e32 v57, 0x37800000, v55
	v_cndmask_b32_e32 v55, v55, v57, vcc
	v_cmp_class_f32_e32 vcc, v54, v229
	s_nop 1
	v_cndmask_b32_e32 v54, v55, v54, vcc
	v_max_f32_e32 v54, 0x2b8cbccc, v54
	v_div_scale_f32 v55, s[4:5], v54, v54, 1.0
	v_rcp_f32_e32 v57, v55
	s_nop 0
	v_fma_f32 v92, -v55, v57, 1.0
	v_fmac_f32_e32 v57, v92, v57
	v_div_scale_f32 v92, vcc, 1.0, v54, 1.0
	v_mul_f32_e32 v93, v92, v57
	v_fma_f32 v94, -v55, v93, v92
	v_fmac_f32_e32 v93, v94, v57
	v_fma_f32 v55, -v55, v93, v92
	v_div_fmas_f32 v55, v55, v57, v93
	v_div_fixup_f32 v54, v55, v54, 1.0
	v_mul_f32_e32 v55, v56, v54
	v_mul_f32_e32 v56, v89, v54
	v_mul_f32_e32 v57, v88, v54
	v_mul_f32_e32 v44, v44, v54
	v_mul_f32_e32 v45, v45, v54
	v_mul_f32_e32 v0, v0, v54
	v_mul_f32_e32 v48, v48, v54
	v_mul_f32_e32 v49, v49, v54
	v_cvt_pk_bf16_f32 v54, v0, v55
	v_cvt_pk_bf16_f32 v55, v56, v57
	v_cvt_pk_bf16_f32 v56, v48, v49
	v_cvt_pk_bf16_f32 v57, v44, v45
	v_lshl_add_u64 v[44:45], s[50:51], 0, v[84:85]
	v_add_co_u32_e32 v44, vcc, 0x2e20b000, v44
	s_nop 1
	v_addc_co_u32_e32 v45, vcc, 0, v45, vcc
	global_store_dwordx4 v[44:45], v[54:57], off offset:2048 sc1

.LBB0_713:
	s_and_b64 vcc, exec, s[4:5]
	s_cbranch_vccz .LBB0_716
	v_add_co_u32_e32 v54, vcc, 0x2e20c000, v62
	v_cvt_pk_bf16_f32 v50, v0, v44
	v_cvt_pk_bf16_f32 v51, v45, v48
	v_cvt_pk_bf16_f32 v52, v38, v39
	v_cvt_pk_bf16_f32 v53, v40, v41
	s_nop 1
	v_addc_co_u32_e32 v55, vcc, 0, v63, vcc
	s_and_b64 vcc, exec, s[42:43]
	global_store_dwordx4 v[54:55], v[50:53], off sc1
	s_cbranch_vccnz .LBB0_716
	v_mul_f32_e32 v49, v103, v44
	v_mul_f32_e32 v0, v104, v0
	v_mul_f32_e32 v50, v49, v49
	v_fmac_f32_e32 v50, v0, v0
	v_mul_f32_e32 v51, v110, v45
	v_fmac_f32_e32 v50, v51, v51
	v_mul_f32_e32 v48, v109, v48
	v_pk_mul_f32 v[38:39], v[72:73], v[38:39]
	v_fmac_f32_e32 v50, v48, v48
	v_pk_mul_f32 v[44:45], v[38:39], v[38:39]
	v_pk_mul_f32 v[40:41], v[78:79], v[40:41]
	v_add_f32_e32 v44, v44, v50
	v_add_f32_e32 v50, v45, v44
	v_pk_mul_f32 v[44:45], v[40:41], v[40:41]
	s_nop 0
	v_add_f32_e32 v44, v44, v50
	v_and_b32_e32 v50, 64, v226
	v_add_f32_e32 v44, v45, v44
	v_xor_b32_e32 v45, 1, v226
	v_add_u32_e32 v50, 64, v50
	v_cmp_lt_i32_e32 vcc, v45, v50
	s_nop 1
	v_cndmask_b32_e32 v45, v226, v45, vcc
	v_lshlrev_b32_e32 v45, 2, v45
	v_mov_b32_dpp v45, v44 quad_perm:[1,0,3,2] row_mask:0xf bank_mask:0xf
	s_waitcnt lgkmcnt(0)
	v_add_f32_e32 v44, v44, v45
	s_nop 1
	v_mov_b32_dpp v45, v44 quad_perm:[2,3,0,1] row_mask:0xf bank_mask:0xf
	s_waitcnt lgkmcnt(0)
	v_add_f32_e32 v44, v44, v45
	s_nop 1
	v_mov_b32_dpp v45, v44 row_half_mirror row_mask:0xf bank_mask:0xf
	s_waitcnt lgkmcnt(0)
	v_add_f32_e32 v44, v44, v45
	v_mul_f32_e32 v45, 0x4f800000, v44
	v_cmp_gt_f32_e32 vcc, s82, v44
	s_nop 1
	v_cndmask_b32_e32 v44, v44, v45, vcc
	v_sqrt_f32_e32 v45, v44
	s_nop 0
	v_add_u32_e32 v50, -1, v45
	v_fma_f32 v52, -v50, v45, v44
	v_cmp_ge_f32_e64 s[46:47], 0, v52
	v_add_u32_e32 v52, 1, v45
	s_nop 0
	v_cndmask_b32_e64 v50, v45, v50, s[46:47]
	v_fma_f32 v45, -v52, v45, v44
	v_cmp_lt_f32_e64 s[46:47], 0, v45
	s_nop 1
	v_cndmask_b32_e64 v45, v50, v52, s[46:47]
	v_mul_f32_e32 v50, 0x37800000, v45
	v_cndmask_b32_e32 v45, v45, v50, vcc
	v_cmp_class_f32_e32 vcc, v44, v229
	s_nop 1
	v_cndmask_b32_e32 v44, v45, v44, vcc
	v_max_f32_e32 v44, 0x2b8cbccc, v44
	v_div_scale_f32 v45, s[4:5], v44, v44, 1.0
	v_rcp_f32_e32 v50, v45
	s_nop 0
	v_fma_f32 v52, -v45, v50, 1.0
	v_fmac_f32_e32 v50, v52, v50
	v_div_scale_f32 v52, vcc, 1.0, v44, 1.0
	v_mul_f32_e32 v53, v52, v50
	v_fma_f32 v54, -v45, v53, v52
	v_fmac_f32_e32 v53, v54, v50
	v_fma_f32 v45, -v45, v53, v52
	v_div_fmas_f32 v45, v45, v50, v53
	v_div_fixup_f32 v44, v45, v44, 1.0
	v_mul_f32_e32 v45, v49, v44
	v_mul_f32_e32 v0, v0, v44
	v_mul_f32_e32 v49, v51, v44
	v_mul_f32_e32 v48, v48, v44
	v_mul_f32_e32 v50, v38, v44
	v_mul_f32_e32 v51, v39, v44
	v_mul_f32_e32 v52, v40, v44
	v_mul_f32_e32 v41, v41, v44
	v_cvt_pk_bf16_f32 v38, v0, v45
	v_lshl_add_u64 v[44:45], s[50:51], 0, v[84:85]
	v_add_co_u32_e32 v44, vcc, 0x2e20d000, v44
	v_cvt_pk_bf16_f32 v39, v49, v48
	v_cvt_pk_bf16_f32 v40, v50, v51
	v_cvt_pk_bf16_f32 v41, v52, v41
	s_nop 1
	v_addc_co_u32_e32 v45, vcc, 0, v45, vcc
	global_store_dwordx4 v[44:45], v[38:41], off offset:2048 sc1

.LBB0_750:
	s_and_b64 vcc, exec, s[4:5]
	s_cbranch_vccz .LBB0_454
	v_add_co_u32_e32 v46, vcc, 0x2e20e000, v62
	v_cvt_pk_bf16_f32 v42, v38, v39
	v_cvt_pk_bf16_f32 v43, v40, v41
	v_cvt_pk_bf16_f32 v44, v34, v35
	v_cvt_pk_bf16_f32 v45, v36, v37
	s_nop 1
	v_addc_co_u32_e32 v47, vcc, 0, v63, vcc
	s_and_b64 vcc, exec, s[42:43]
	global_store_dwordx4 v[46:47], v[42:45], off sc1
	s_cbranch_vccnz .LBB0_454
	s_nop 0
	v_mul_f32_e32 v43, v103, v39
	v_mul_f32_e32 v42, v104, v38
	v_mul_f32_e32 v44, v43, v43
	v_fmac_f32_e32 v44, v42, v42
	v_mul_f32_e32 v40, v110, v40
	v_fmac_f32_e32 v44, v40, v40
	v_mul_f32_e32 v41, v109, v41
	v_pk_mul_f32 v[34:35], v[72:73], v[34:35]
	v_fmac_f32_e32 v44, v41, v41
	v_pk_mul_f32 v[38:39], v[34:35], v[34:35]
	v_pk_mul_f32 v[36:37], v[78:79], v[36:37]
	v_add_f32_e32 v38, v38, v44
	v_add_f32_e32 v44, v39, v38
	v_pk_mul_f32 v[38:39], v[36:37], v[36:37]
	s_nop 0
	v_add_f32_e32 v38, v38, v44
	v_and_b32_e32 v44, 64, v226
	v_add_f32_e32 v38, v39, v38
	v_xor_b32_e32 v39, 1, v226
	v_add_u32_e32 v44, 64, v44
	v_cmp_lt_i32_e32 vcc, v39, v44
	s_nop 1
	v_cndmask_b32_e32 v39, v226, v39, vcc
	v_lshlrev_b32_e32 v39, 2, v39
	v_mov_b32_dpp v39, v38 quad_perm:[1,0,3,2] row_mask:0xf bank_mask:0xf
	s_waitcnt lgkmcnt(0)
	v_add_f32_e32 v38, v38, v39
	s_nop 1
	v_mov_b32_dpp v39, v38 quad_perm:[2,3,0,1] row_mask:0xf bank_mask:0xf
	s_waitcnt lgkmcnt(0)
	v_add_f32_e32 v38, v38, v39
	s_nop 1
	v_mov_b32_dpp v39, v38 row_half_mirror row_mask:0xf bank_mask:0xf
	s_waitcnt lgkmcnt(0)
	v_add_f32_e32 v38, v38, v39
	v_mul_f32_e32 v39, 0x4f800000, v38
	v_cmp_gt_f32_e32 vcc, s82, v38
	s_nop 1
	v_cndmask_b32_e32 v38, v38, v39, vcc
	v_sqrt_f32_e32 v39, v38
	s_nop 0
	v_add_u32_e32 v44, -1, v39
	v_fma_f32 v45, -v44, v39, v38
	v_cmp_ge_f32_e64 s[42:43], 0, v45
	v_add_u32_e32 v45, 1, v39
	s_nop 0
	v_cndmask_b32_e64 v44, v39, v44, s[42:43]
	v_fma_f32 v39, -v45, v39, v38
	v_cmp_lt_f32_e64 s[42:43], 0, v39
	s_nop 1
	v_cndmask_b32_e64 v39, v44, v45, s[42:43]
	v_mul_f32_e32 v44, 0x37800000, v39
	v_cndmask_b32_e32 v39, v39, v44, vcc
	v_cmp_class_f32_e32 vcc, v38, v229
	s_nop 1
	v_cndmask_b32_e32 v38, v39, v38, vcc
	v_max_f32_e32 v38, 0x2b8cbccc, v38
	v_div_scale_f32 v39, s[4:5], v38, v38, 1.0
	v_rcp_f32_e32 v44, v39
	s_nop 0
	v_fma_f32 v45, -v39, v44, 1.0
	v_fmac_f32_e32 v44, v45, v44
	v_div_scale_f32 v45, vcc, 1.0, v38, 1.0
	v_mul_f32_e32 v46, v45, v44
	v_fma_f32 v47, -v39, v46, v45
	v_fmac_f32_e32 v46, v47, v44
	v_fma_f32 v39, -v39, v46, v45
	v_div_fmas_f32 v39, v39, v44, v46
	v_div_fixup_f32 v38, v39, v38, 1.0
	v_mul_f32_e32 v39, v42, v38
	v_mul_f32_e32 v42, v43, v38
	v_mul_f32_e32 v40, v40, v38
	v_mul_f32_e32 v41, v41, v38
	v_mul_f32_e32 v43, v34, v38
	v_mul_f32_e32 v44, v35, v38
	v_mul_f32_e32 v45, v36, v38
	v_mul_f32_e32 v37, v37, v38
	v_cvt_pk_bf16_f32 v34, v39, v42
	v_lshl_add_u64 v[38:39], s[50:51], 0, v[84:85]
	v_add_co_u32_e32 v38, vcc, 0x2e20f000, v38
	v_cvt_pk_bf16_f32 v35, v40, v41
	v_cvt_pk_bf16_f32 v36, v43, v44
	v_cvt_pk_bf16_f32 v37, v45, v37
	s_nop 1
	v_addc_co_u32_e32 v39, vcc, 0, v39, vcc
	global_store_dwordx4 v[38:39], v[34:37], off offset:2048 sc1
	s_branch .LBB0_454
